# speedup vs baseline: 1.0106x; 1.0106x over previous
_Z11gemm_kernelILi2EEvPKDF16_S1_PKfPDF16_PfS5_S3_S3_S1_S3_:
	s_load_dwordx4 s[8:11], s[0:1], 0x28
	s_load_dwordx4 s[4:7], s[0:1], 0x0
	v_mov_b32_e32 v211, 0
	v_lshlrev_b32_e32 v178, 2, v0
	v_mov_b32_e32 v179, v211
	s_waitcnt lgkmcnt(0)
	v_lshl_add_u64 v[2:3], s[8:9], 0, v[178:179]
	s_movk_i32 s3, 0x1000
	v_add_co_u32_e32 v4, vcc, s3, v2
	s_movk_i32 s14, 0x2000
	s_nop 0
	v_addc_co_u32_e32 v5, vcc, 0, v3, vcc
	v_add_co_u32_e32 v6, vcc, s14, v2
	s_movk_i32 s15, 0x3000
	s_nop 0
	v_addc_co_u32_e32 v7, vcc, 0, v3, vcc
	global_load_dword v46, v[6:7], off
	global_load_dword v47, v[6:7], off offset:1024
	global_load_dword v48, v[6:7], off offset:2048
	global_load_dword v49, v[6:7], off offset:3072
	v_add_co_u32_e32 v2, vcc, s15, v2
	v_lshrrev_b32_e32 v1, 6, v0
	s_nop 0
	v_addc_co_u32_e32 v3, vcc, 0, v3, vcc
	global_load_dword v50, v[2:3], off
	global_load_dword v51, v[2:3], off offset:1024
	global_load_dword v52, v[2:3], off offset:2048
	global_load_dword v53, v[2:3], off offset:3072
	s_load_dwordx2 s[8:9], s[0:1], 0x48
	s_load_dwordx2 s[12:13], s[0:1], 0x38
	global_load_dword v54, v178, s[10:11]
	s_waitcnt lgkmcnt(0)
	global_load_dword v112, v178, s[8:9]
	global_load_dword v120, v178, s[12:13]
	v_lshlrev_b32_e32 v2, 4, v0
	v_and_b32_e32 v2, 0x3f0, v2
	v_lshl_or_b32 v210, v1, 15, v2
	v_lshl_add_u64 v[94:95], s[6:7], 0, v[210:211]
	v_add_co_u32_e32 v42, vcc, s3, v94
	s_movk_i32 s9, 0x4000
	s_nop 0
	v_addc_co_u32_e32 v43, vcc, 0, v95, vcc
	v_add_co_u32_e32 v34, vcc, s14, v94
	s_mov_b32 s8, 0x800000
	s_nop 0
	v_addc_co_u32_e32 v35, vcc, 0, v95, vcc
	v_add_co_u32_e32 v66, vcc, s15, v94
	s_movk_i32 s3, 0x5000
	s_nop 0
	v_addc_co_u32_e32 v67, vcc, 0, v95, vcc
	v_add_co_u32_e32 v68, vcc, s9, v94
	v_lshrrev_b32_e32 v180, 5, v0
	s_nop 0
	v_addc_co_u32_e32 v69, vcc, 0, v95, vcc
	global_load_dwordx4 v[2:5], v[42:43], off offset:1024
	global_load_dwordx4 v[6:9], v[42:43], off offset:2048
	global_load_dwordx4 v[10:13], v[34:35], off offset:-4096
	global_load_dwordx4 v[14:17], v[34:35], off
	global_load_dwordx4 v[18:21], v[34:35], off offset:1024
	global_load_dwordx4 v[22:25], v[34:35], off offset:2048
	global_load_dwordx4 v[26:29], v[34:35], off offset:3072
	global_load_dwordx4 v[30:33], v[68:69], off offset:-4096
	v_and_b32_e32 v179, 31, v0
	v_lshlrev_b32_e32 v142, 5, v179
	s_waitcnt vmcnt(18)
	v_add_f32_e32 v34, 0, v46
	s_waitcnt vmcnt(17)
	v_add_f32_e32 v35, 0, v47
	s_waitcnt vmcnt(16)
	v_add_f32_e32 v34, v34, v48
	s_waitcnt vmcnt(15)
	v_add_f32_e32 v35, v35, v49
	s_waitcnt vmcnt(14)
	v_add_f32_e32 v34, v34, v50
	s_waitcnt vmcnt(13)
	v_add_f32_e32 v35, v35, v51
	s_waitcnt vmcnt(12)
	v_add_f32_e32 v44, v34, v52
	s_waitcnt vmcnt(11)
	v_add_f32_e32 v34, v35, v53
	v_mul_f32_e32 v35, 0x37a7c5ac, v44
	v_mul_f32_e32 v34, 0x37a7c5ac, v34
	v_fma_f32 v34, -v35, v35, v34
	v_add_f32_e32 v34, 0x3727c5ac, v34
	v_mul_f32_e32 v35, 0x4b800000, v34
	v_cmp_gt_f32_e32 vcc, s8, v34
	s_waitcnt vmcnt(9)
	v_fmamk_f32 v113, v44, 0x37a7c5ac, v112
	v_cndmask_b32_e32 v34, v34, v35, vcc
	v_rsq_f32_e32 v45, v34
	global_load_dwordx4 v[34:37], v[42:43], off offset:3072
	global_load_dwordx4 v[38:41], v[66:67], off offset:1024
	v_mul_f32_e32 v42, 0x45800000, v45
	v_cndmask_b32_e32 v42, v45, v42, vcc
	v_add_co_u32_e32 v110, vcc, s3, v94
	s_movk_i32 s3, 0x6000
	s_nop 0
	v_addc_co_u32_e32 v111, vcc, 0, v95, vcc
	v_add_co_u32_e32 v96, vcc, s3, v94
	s_movk_i32 s3, 0x7000
	s_nop 0
	v_addc_co_u32_e32 v97, vcc, 0, v95, vcc
	v_add_co_u32_e32 v118, vcc, s3, v94
	v_mul_f32_e32 v121, v42, v54
	global_load_dwordx4 v[42:45], v[66:67], off offset:2048
	global_load_dwordx4 v[46:49], v[66:67], off offset:3072
	global_load_dwordx4 v[50:53], v[68:69], off
	global_load_dwordx4 v[54:57], v[68:69], off offset:1024
	global_load_dwordx4 v[58:61], v[68:69], off offset:2048
	global_load_dwordx4 v[62:65], v[68:69], off offset:3072
	s_nop 0
	global_load_dwordx4 v[66:69], v[110:111], off offset:1024
	global_load_dwordx4 v[70:73], v[110:111], off offset:2048
	global_load_dwordx4 v[74:77], v[96:97], off offset:-4096
	global_load_dwordx4 v[78:81], v[96:97], off
	global_load_dwordx4 v[82:85], v[96:97], off offset:1024
	global_load_dwordx4 v[86:89], v[96:97], off offset:2048
	global_load_dwordx4 v[90:93], v[96:97], off offset:3072
	v_addc_co_u32_e32 v119, vcc, 0, v95, vcc
	global_load_dwordx4 v[94:97], v[110:111], off offset:3072
	global_load_dwordx4 v[98:101], v[118:119], off
	global_load_dwordx4 v[102:105], v[118:119], off offset:1024
	global_load_dwordx4 v[106:109], v[118:119], off offset:2048
	v_sub_f32_e32 v110, v112, v113
	s_waitcnt vmcnt(27)
	v_fmac_f32_e32 v120, v110, v121
	global_load_dwordx4 v[110:113], v210, s[6:7]
	global_load_dwordx4 v[114:117], v[118:119], off offset:3072
	ds_write2st64_b32 v178, v121, v120 offset1:4
	global_load_dwordx4 v[118:121], v210, s[6:7] offset:1024
	global_load_dwordx4 v[122:125], v210, s[6:7] offset:2048
	global_load_dwordx4 v[126:129], v210, s[6:7] offset:3072
	s_lshl_b32 s6, s2, 5
	v_or_b32_e32 v158, s6, v180
	v_min_i32_e32 v146, 0xc34f, v158
	v_ashrrev_i32_e32 v147, 31, v146
	v_lshlrev_b64 v[146:147], 9, v[146:147]
	v_lshl_add_u64 v[146:147], s[4:5], 0, v[146:147]
	v_lshlrev_b32_e32 v210, 4, v179
	v_lshl_add_u64 v[146:147], v[146:147], 0, v[210:211]
	s_waitcnt lgkmcnt(0)
	s_barrier
	ds_read_b128 v[130:133], v142
	ds_read_b128 v[134:137], v142 offset:16
	ds_read_b128 v[138:141], v142 offset:1024
	ds_read_b128 v[142:145], v142 offset:1040
	s_waitcnt lgkmcnt(0)
	s_barrier
	global_load_dwordx4 v[146:149], v[146:147], off nt
	v_or_b32_e32 v150, 8, v158
	v_min_i32_e32 v150, 0xc34f, v150
	v_ashrrev_i32_e32 v151, 31, v150
	v_lshlrev_b64 v[150:151], 9, v[150:151]
	v_lshl_add_u64 v[150:151], s[4:5], 0, v[150:151]
	v_lshl_add_u64 v[150:151], v[150:151], 0, v[210:211]
	global_load_dwordx4 v[150:153], v[150:151], off nt
	v_or_b32_e32 v154, 16, v158
	v_min_i32_e32 v154, 0xc34f, v154
	v_ashrrev_i32_e32 v155, 31, v154
	v_lshlrev_b64 v[154:155], 9, v[154:155]
	v_lshl_add_u64 v[154:155], s[4:5], 0, v[154:155]
	v_lshl_add_u64 v[154:155], v[154:155], 0, v[210:211]
	global_load_dwordx4 v[154:157], v[154:155], off nt
	v_or_b32_e32 v158, 24, v158
	v_min_i32_e32 v158, 0xc34f, v158
	v_ashrrev_i32_e32 v159, 31, v158
	v_lshlrev_b64 v[158:159], 9, v[158:159]
	v_lshl_add_u64 v[158:159], s[4:5], 0, v[158:159]
	v_lshl_add_u64 v[158:159], v[158:159], 0, v[210:211]
	global_load_dwordx4 v[158:161], v[158:159], off nt
	s_movk_i32 s7, 0x210
	v_mad_u32_u24 v216, v180, s7, v210
	s_mov_b32 s3, 0
	s_cmpk_gt_i32 s2, 0x61a
	s_waitcnt vmcnt(3)
	v_cvt_f32_f16_e32 v162, v146
	v_cvt_f32_f16_sdwa v163, v146 dst_sel:DWORD dst_unused:UNUSED_PAD src0_sel:WORD_1
	v_cvt_f32_f16_e32 v164, v147
	v_cvt_f32_f16_sdwa v165, v147 dst_sel:DWORD dst_unused:UNUSED_PAD src0_sel:WORD_1
	v_pk_fma_f32 v[162:163], v[130:131], v[162:163], v[138:139]
	s_nop 0
	v_max_f32_e32 v166, 0, v163
	v_max_f32_e32 v167, 0, v162
	v_pk_fma_f32 v[162:163], v[132:133], v[164:165], v[140:141]
	v_cvt_f32_f16_e32 v164, v148
	v_cvt_f32_f16_sdwa v165, v148 dst_sel:DWORD dst_unused:UNUSED_PAD src0_sel:WORD_1
	v_max_f32_e32 v168, 0, v162
	v_cvt_pk_f16_f32 v162, v167, v166
	v_cvt_f32_f16_e32 v166, v149
	v_cvt_f32_f16_sdwa v167, v149 dst_sel:DWORD dst_unused:UNUSED_PAD src0_sel:WORD_1
	v_pk_fma_f32 v[164:165], v[134:135], v[164:165], v[142:143]
	v_max_f32_e32 v163, 0, v163
	v_max_f32_e32 v165, 0, v165
	v_max_f32_e32 v164, 0, v164
	v_pk_fma_f32 v[166:167], v[136:137], v[166:167], v[144:145]
	v_cvt_pk_f16_f32 v164, v164, v165
	v_max_f32_e32 v165, 0, v167
	v_max_f32_e32 v166, 0, v166
	v_cvt_pk_f16_f32 v163, v168, v163
	v_cvt_pk_f16_f32 v165, v166, v165
	s_waitcnt vmcnt(2)
	v_cvt_f32_f16_e32 v166, v150
	v_cvt_f32_f16_sdwa v167, v150 dst_sel:DWORD dst_unused:UNUSED_PAD src0_sel:WORD_1
	ds_write_b128 v216, v[162:165]
	v_cvt_f32_f16_e32 v162, v151
	v_cvt_f32_f16_sdwa v163, v151 dst_sel:DWORD dst_unused:UNUSED_PAD src0_sel:WORD_1
	v_pk_fma_f32 v[164:165], v[130:131], v[166:167], v[138:139]
	v_pk_fma_f32 v[162:163], v[132:133], v[162:163], v[140:141]
	v_max_f32_e32 v166, 0, v165
	v_max_f32_e32 v167, 0, v164
	v_cvt_f32_f16_e32 v164, v152
	v_cvt_f32_f16_sdwa v165, v152 dst_sel:DWORD dst_unused:UNUSED_PAD src0_sel:WORD_1
	v_max_f32_e32 v168, 0, v162
	v_cvt_pk_f16_f32 v162, v167, v166
	v_cvt_f32_f16_e32 v166, v153
	v_cvt_f32_f16_sdwa v167, v153 dst_sel:DWORD dst_unused:UNUSED_PAD src0_sel:WORD_1
	v_pk_fma_f32 v[164:165], v[134:135], v[164:165], v[142:143]
	v_max_f32_e32 v163, 0, v163
	v_max_f32_e32 v165, 0, v165
	v_max_f32_e32 v164, 0, v164
	v_pk_fma_f32 v[166:167], v[136:137], v[166:167], v[144:145]
	v_cvt_pk_f16_f32 v164, v164, v165
	v_max_f32_e32 v165, 0, v167
	v_max_f32_e32 v166, 0, v166
	v_cvt_pk_f16_f32 v163, v168, v163
	v_cvt_pk_f16_f32 v165, v166, v165
	s_waitcnt vmcnt(1)
	v_cvt_f32_f16_e32 v166, v154
	v_cvt_f32_f16_sdwa v167, v154 dst_sel:DWORD dst_unused:UNUSED_PAD src0_sel:WORD_1
	ds_write_b128 v216, v[162:165] offset:4224
	v_cvt_f32_f16_e32 v162, v155
	v_cvt_f32_f16_sdwa v163, v155 dst_sel:DWORD dst_unused:UNUSED_PAD src0_sel:WORD_1
	v_pk_fma_f32 v[164:165], v[130:131], v[166:167], v[138:139]
	v_pk_fma_f32 v[162:163], v[132:133], v[162:163], v[140:141]
	v_max_f32_e32 v166, 0, v165
	v_max_f32_e32 v167, 0, v164
	v_cvt_f32_f16_e32 v164, v156
	v_cvt_f32_f16_sdwa v165, v156 dst_sel:DWORD dst_unused:UNUSED_PAD src0_sel:WORD_1
	v_max_f32_e32 v168, 0, v162
	v_cvt_pk_f16_f32 v162, v167, v166
	v_cvt_f32_f16_e32 v166, v157
	v_cvt_f32_f16_sdwa v167, v157 dst_sel:DWORD dst_unused:UNUSED_PAD src0_sel:WORD_1
	v_pk_fma_f32 v[164:165], v[134:135], v[164:165], v[142:143]
	v_max_f32_e32 v163, 0, v163
	v_max_f32_e32 v165, 0, v165
	v_max_f32_e32 v164, 0, v164
	v_pk_fma_f32 v[166:167], v[136:137], v[166:167], v[144:145]
	v_cvt_pk_f16_f32 v164, v164, v165
	v_max_f32_e32 v165, 0, v167
	v_max_f32_e32 v166, 0, v166
	v_cvt_pk_f16_f32 v163, v168, v163
	v_cvt_pk_f16_f32 v165, v166, v165
	s_waitcnt vmcnt(0)
	v_cvt_f32_f16_e32 v166, v158
	v_cvt_f32_f16_sdwa v167, v158 dst_sel:DWORD dst_unused:UNUSED_PAD src0_sel:WORD_1
	ds_write_b128 v216, v[162:165] offset:8448
	v_cvt_f32_f16_e32 v162, v159
	v_cvt_f32_f16_sdwa v163, v159 dst_sel:DWORD dst_unused:UNUSED_PAD src0_sel:WORD_1
	v_pk_fma_f32 v[164:165], v[130:131], v[166:167], v[138:139]
	v_pk_fma_f32 v[162:163], v[132:133], v[162:163], v[140:141]
	v_max_f32_e32 v166, 0, v165
	v_max_f32_e32 v167, 0, v164
	v_cvt_f32_f16_e32 v164, v160
	v_cvt_f32_f16_sdwa v165, v160 dst_sel:DWORD dst_unused:UNUSED_PAD src0_sel:WORD_1
	v_max_f32_e32 v168, 0, v162
	v_cvt_pk_f16_f32 v162, v167, v166
	v_cvt_f32_f16_e32 v166, v161
	v_cvt_f32_f16_sdwa v167, v161 dst_sel:DWORD dst_unused:UNUSED_PAD src0_sel:WORD_1
	v_pk_fma_f32 v[164:165], v[134:135], v[164:165], v[142:143]
	v_max_f32_e32 v163, 0, v163
	v_max_f32_e32 v165, 0, v165
	v_max_f32_e32 v164, 0, v164
	v_pk_fma_f32 v[166:167], v[136:137], v[166:167], v[144:145]
	v_cvt_pk_f16_f32 v164, v164, v165
	v_max_f32_e32 v165, 0, v167
	v_max_f32_e32 v166, 0, v166
	v_cvt_pk_f16_f32 v163, v168, v163
	v_cvt_pk_f16_f32 v165, v166, v165
	ds_write_b128 v216, v[162:165] offset:12672
	s_waitcnt lgkmcnt(0)
	s_barrier
	s_cbranch_scc1 .LBB3_11
	v_lshrrev_b32_e32 v162, 2, v0
	s_load_dwordx2 s[10:11], s[0:1], 0x10
	s_load_dword s12, s[0:1], 0x50
	s_load_dwordx2 s[8:9], s[0:1], 0x20
	v_and_b32_e32 v181, 12, v162
	s_movk_i32 s13, 0xc0
	v_and_or_b32 v162, v0, s13, v181
	v_lshlrev_b32_e32 v174, 2, v162
	s_waitcnt lgkmcnt(0)
	global_load_dwordx4 v[162:165], v174, s[10:11]
	global_load_dwordx4 v[166:169], v174, s[10:11] offset:64
	global_load_dwordx4 v[170:173], v174, s[10:11] offset:128
	s_nop 0
	global_load_dwordx4 v[174:177], v174, s[10:11] offset:192
	s_load_dwordx2 s[0:1], s[0:1], 0x40
	v_lshlrev_b32_e32 v179, 3, v179
	v_lshlrev_b32_e32 v210, 1, v179
	v_and_b32_e32 v182, 15, v0
	v_lshl_add_u64 v[212:213], s[4:5], 0, v[210:211]
	v_and_b32_e32 v179, 48, v0
	v_mul_u32_u24_e32 v210, 0xc350, v1
	v_lshlrev_b32_e32 v0, 1, v181
	v_mov_b32_e32 v1, v211
	s_waitcnt lgkmcnt(0)
	v_lshl_add_u64 v[0:1], s[0:1], 0, v[0:1]
	s_add_i32 s0, s2, s12
	v_and_b32_e32 v178, 0x300, v178
	v_lshl_or_b32 v218, s0, 5, v180
	s_lshl_b32 s0, s2, 15
	v_lshlrev_b32_e32 v180, 10, v182
	v_or3_b32 v178, s0, v180, v178
	s_movk_i32 s0, 0x40c0
	s_mov_b32 s11, 0x20000
	s_mov_b32 s10, 0x30d4000
	s_and_b32 s9, s9, 0xffff
	s_mov_b32 s13, 0xc350
	v_mad_u32_u24 v217, v182, s7, v179
	s_lshl_b32 s14, s12, 5
	v_add_u32_e32 v219, s6, v182
	v_or3_b32 v220, v178, v179, s0
	s_lshl_b32 s15, s12, 15
	s_mov_b32 s16, 0
	s_branch .LBB3_3
